# P1 K-loop: compiler vmcnt(0) at loop header moved to the entry edge (back edge keeps LDS-DMA loads in flight)
# speedup vs baseline: 1.0059x; 1.0014x over previous
.LBB0_161:
	s_ashr_i32 s31, s30, 31
	s_lshl_b64 s[34:35], s[30:31], 18
	s_add_u32 s34, s27, s34
	s_addc_u32 s35, s58, s35
	s_and_b64 s[40:41], s[38:39], exec
	s_cselect_b32 s7, s35, s45
	s_cselect_b32 s8, s34, s44
	s_ashr_i32 s29, s28, 31
	s_lshl_b64 s[40:41], s[28:29], 18
	s_add_u32 s40, s59, s40
	s_addc_u32 s41, s60, s41
	s_and_b64 s[52:53], s[38:39], exec
	s_cselect_b32 s29, s41, s47
	s_cselect_b32 s31, s40, s46
	s_add_u32 s33, s46, 0x100
	v_lshl_add_u64 v[206:207], s[44:45], 0, v[202:203]
	v_lshl_add_u64 v[208:209], s[44:45], 0, v[204:205]
	s_addc_u32 s43, s47, 0
	s_mov_b32 s78, -2
	s_mov_b64 s[46:47], 0
	s_waitcnt vmcnt(0)
	s_branch .LBB0_163

.LBB0_163:
	v_add_u32_e32 v10, 0, v234
	v_add_u32_e32 v11, 0x10000, v10
	v_add_u32_e32 v30, 0x14000, v10
	ds_read_b128 v[2:5], v11
	ds_read_b128 v[6:9], v11 offset:1024
	ds_read_b128 v[18:21], v11 offset:2048
	ds_read_b128 v[22:25], v11 offset:3072
	ds_read_b128 v[10:13], v30
	ds_read_b128 v[14:17], v30 offset:1024
	ds_read_b128 v[26:29], v30 offset:2048
	ds_read_b128 v[30:33], v30 offset:3072
	v_lshl_add_u64 v[210:211], v[206:207], 0, s[46:47]
	s_add_i32 m0, s62, 0xc000
	ds_read_b128 v[34:37], v238
	ds_read_b128 v[38:41], v238 offset:1024
	ds_read_b128 v[42:45], v238 offset:2048
	ds_read_b128 v[46:49], v238 offset:3072
	ds_read_b128 v[50:53], v238 offset:4096
	ds_read_b128 v[54:57], v238 offset:5120
	ds_read_b128 v[58:61], v238 offset:6144
	ds_read_b128 v[62:65], v238 offset:7168
	global_load_lds_dwordx4 v[210:211], off
	v_lshl_add_u64 v[210:211], v[208:209], 0, s[46:47]
	s_add_i32 m0, s62, 0xe000
	s_cmp_lg_u32 s46, 0
	global_load_lds_dwordx4 v[210:211], off
	s_waitcnt vmcnt(8)
	s_waitcnt lgkmcnt(0)
	s_cselect_b64 s[56:57], -1, 0
	s_barrier
	s_setprio 1
	s_and_b64 vcc, exec, s[56:57]
	s_cbranch_vccz .LBB0_168
	s_waitcnt lgkmcnt(0)
	v_mfma_scale_f32_16x16x128_f8f6f4 v[106:109], v[2:9], v[34:41], v[106:109], v236, v237 op_sel_hi:[0,0,0]
	v_mfma_scale_f32_16x16x128_f8f6f4 v[122:125], v[18:25], v[34:41], v[122:125], v236, v237 op_sel_hi:[0,0,0]
	v_mfma_scale_f32_16x16x128_f8f6f4 v[134:137], v[2:9], v[42:49], v[134:137], v236, v237 op_sel_hi:[0,0,0]
	v_mfma_scale_f32_16x16x128_f8f6f4 v[146:149], v[18:25], v[42:49], v[146:149], v236, v237 op_sel_hi:[0,0,0]
	v_mfma_scale_f32_16x16x128_f8f6f4 v[158:161], v[2:9], v[50:57], v[158:161], v236, v237 op_sel_hi:[0,0,0]
	v_mfma_scale_f32_16x16x128_f8f6f4 v[114:117], v[18:25], v[50:57], v[114:117], v236, v237 op_sel_hi:[0,0,0]
	v_mfma_scale_f32_16x16x128_f8f6f4 v[126:129], v[2:9], v[58:65], v[126:129], v236, v237 op_sel_hi:[0,0,0]
	v_mfma_scale_f32_16x16x128_f8f6f4 v[138:141], v[18:25], v[58:65], v[138:141], v236, v237 op_sel_hi:[0,0,0]
	s_setprio 0
	s_setprio 1
	v_mfma_scale_f32_16x16x128_f8f6f4 v[162:165], v[10:17], v[34:41], v[162:165], v236, v237 op_sel_hi:[0,0,0]
	v_mfma_scale_f32_16x16x128_f8f6f4 v[166:169], v[26:33], v[34:41], v[166:169], v236, v237 op_sel_hi:[0,0,0]
	v_mfma_scale_f32_16x16x128_f8f6f4 v[170:173], v[10:17], v[42:49], v[170:173], v236, v237 op_sel_hi:[0,0,0]
	v_mfma_scale_f32_16x16x128_f8f6f4 v[174:177], v[26:33], v[42:49], v[174:177], v236, v237 op_sel_hi:[0,0,0]
	v_mfma_scale_f32_16x16x128_f8f6f4 v[178:181], v[10:17], v[50:57], v[178:181], v236, v237 op_sel_hi:[0,0,0]
	v_mfma_scale_f32_16x16x128_f8f6f4 v[182:185], v[26:33], v[50:57], v[182:185], v236, v237 op_sel_hi:[0,0,0]
	v_mfma_scale_f32_16x16x128_f8f6f4 v[186:189], v[10:17], v[58:65], v[186:189], v236, v237 op_sel_hi:[0,0,0]
	v_mfma_scale_f32_16x16x128_f8f6f4 v[190:193], v[26:33], v[58:65], v[190:193], v236, v237 op_sel_hi:[0,0,0]
	s_cbranch_execnz .LBB0_166
